# v8s + hand-written meta-row attention (rows 64..127 of each (b,head): zero padding rows, 16 meta rows by f32 VALU dot products / softmax / PV on 64 workgroups, replacing the scalar-FMA LDS-staged body
# baseline (speedup 1.0000x reference)
.LBB0_1250:
	s_cmpk_lt_i32 s67, 0x1080
	s_mov_b32 s60, s78
	s_waitcnt vmcnt(0) lgkmcnt(0)
	s_barrier
	v_mbcnt_lo_u32_b32 v20, -1, 0
	v_mbcnt_hi_u32_b32 v20, -1, v20
	s_cbranch_scc0 .LBB0_1259
	s_cmp_gt_u32 s67, 63
	s_cbranch_scc1 .LBB0_1259
	v_readlane_b32 s7, v250, 43
	v_readlane_b32 s20, v250, 46
	v_readlane_b32 s21, v250, 47
	v_readlane_b32 s36, v250, 48
	v_readlane_b32 s37, v250, 49
	s_lshr_b32 s28, s67, 4
	s_and_b32 s29, s67, 15
	s_mul_i32 s30, s28, 0x1080
	s_lshl_b32 s29, s29, 8
	s_mul_i32 s33, s67, 0x4200
	s_add_u32 s42, s74, s33
	s_addc_u32 s43, s75, 0
	s_add_u32 s42, s42, 0x500000
	s_addc_u32 s43, s43, 0
	s_lshl_b32 s33, s7, 3
	s_add_i32 s33, s33, 0x1c0
	v_mov_b32_e32 v54, s33
	global_load_dwordx2 v[18:19], v54, s[42:43]
	v_lshrrev_b32_e32 v55, 2, v20
	v_lshlrev_b32_e32 v56, 2, v55
	global_load_dword v57, v56, s[42:43] offset:448
	s_add_i32 s31, s30, 0x70
	s_lshl_b32 s31, s31, 12
	s_add_i32 s31, s31, s29
	v_and_b32_e32 v58, 3, v20
	v_lshlrev_b32_e32 v58, 6, v58
	v_lshl_add_u32 v59, v55, 12, v58
	v_add_u32_e32 v59, s31, v59
	global_load_dwordx4 v[2:5], v59, s[24:25]
	global_load_dwordx4 v[6:9], v59, s[24:25] offset:16
	global_load_dwordx4 v[10:13], v59, s[24:25] offset:32
	global_load_dwordx4 v[14:17], v59, s[24:25] offset:48
	s_lshl_b32 s34, s7, 13
	s_add_i32 s34, s34, s31
	v_add_u32_e32 v60, s34, v58
	v_add_u32_e32 v61, 0x1000, v60
	global_load_dwordx4 v[22:25], v60, s[20:21]
	global_load_dwordx4 v[26:29], v60, s[20:21] offset:16
	global_load_dwordx4 v[30:33], v60, s[20:21] offset:32
	global_load_dwordx4 v[34:37], v60, s[20:21] offset:48
	global_load_dwordx4 v[38:41], v61, s[20:21]
	global_load_dwordx4 v[42:45], v61, s[20:21] offset:16
	global_load_dwordx4 v[46:49], v61, s[20:21] offset:32
	global_load_dwordx4 v[50:53], v61, s[20:21] offset:48
	v_lshlrev_b32_e32 v62, 2, v20
	v_add_u32_e32 v62, s31, v62
	global_load_dword v64, v62, s[26:27]
	v_add_u32_e32 v62, 0x1000, v62
	global_load_dword v65, v62, s[26:27]
	v_add_u32_e32 v62, 0x1000, v62
	global_load_dword v66, v62, s[26:27]
	v_add_u32_e32 v62, 0x1000, v62
	global_load_dword v67, v62, s[26:27]
	v_add_u32_e32 v62, 0x1000, v62
	global_load_dword v68, v62, s[26:27]
	v_add_u32_e32 v62, 0x1000, v62
	global_load_dword v69, v62, s[26:27]
	v_add_u32_e32 v62, 0x1000, v62
	global_load_dword v70, v62, s[26:27]
	v_add_u32_e32 v62, 0x1000, v62
	global_load_dword v71, v62, s[26:27]
	v_add_u32_e32 v62, 0x1000, v62
	global_load_dword v72, v62, s[26:27]
	v_add_u32_e32 v62, 0x1000, v62
	global_load_dword v73, v62, s[26:27]
	v_add_u32_e32 v62, 0x1000, v62
	global_load_dword v74, v62, s[26:27]
	v_add_u32_e32 v62, 0x1000, v62
	global_load_dword v75, v62, s[26:27]
	v_add_u32_e32 v62, 0x1000, v62
	global_load_dword v76, v62, s[26:27]
	v_add_u32_e32 v62, 0x1000, v62
	global_load_dword v77, v62, s[26:27]
	v_add_u32_e32 v62, 0x1000, v62
	global_load_dword v78, v62, s[26:27]
	v_add_u32_e32 v62, 0x1000, v62
	global_load_dword v79, v62, s[26:27]
	s_mul_i32 s35, s7, 6
	s_add_i32 s35, s35, s30
	s_add_i32 s35, s35, 64
	s_lshl_b32 s35, s35, 12
	s_add_i32 s35, s35, s29
	v_lshlrev_b32_e32 v63, 2, v20
	v_add_u32_e32 v63, s35, v63
	v_mov_b32_e32 v80, 0
	global_store_dword v63, v80, s[36:37]
	v_add_u32_e32 v63, 0x1000, v63
	global_store_dword v63, v80, s[36:37]
	v_add_u32_e32 v63, 0x1000, v63
	global_store_dword v63, v80, s[36:37]
	v_add_u32_e32 v63, 0x1000, v63
	global_store_dword v63, v80, s[36:37]
	v_add_u32_e32 v63, 0x1000, v63
	global_store_dword v63, v80, s[36:37]
	v_add_u32_e32 v63, 0x1000, v63
	global_store_dword v63, v80, s[36:37]
	s_waitcnt vmcnt(0)
	v_mov_b32_e32 v81, 0
	v_mov_b32_e32 v82, 0
	v_lshlrev_b32_e32 v83, 16, v2
	v_and_b32_e32 v84, 0xffff0000, v2
	v_lshlrev_b32_e32 v85, 16, v22
	v_and_b32_e32 v86, 0xffff0000, v22
	v_fmac_f32_e32 v81, v83, v85
	v_fmac_f32_e32 v81, v84, v86
	v_lshlrev_b32_e32 v85, 16, v38
	v_and_b32_e32 v86, 0xffff0000, v38
	v_fmac_f32_e32 v82, v83, v85
	v_fmac_f32_e32 v82, v84, v86
	v_lshlrev_b32_e32 v83, 16, v3
	v_and_b32_e32 v84, 0xffff0000, v3
	v_lshlrev_b32_e32 v85, 16, v23
	v_and_b32_e32 v86, 0xffff0000, v23
	v_fmac_f32_e32 v81, v83, v85
	v_fmac_f32_e32 v81, v84, v86
	v_lshlrev_b32_e32 v85, 16, v39
	v_and_b32_e32 v86, 0xffff0000, v39
	v_fmac_f32_e32 v82, v83, v85
	v_fmac_f32_e32 v82, v84, v86
	v_lshlrev_b32_e32 v83, 16, v4
	v_and_b32_e32 v84, 0xffff0000, v4
	v_lshlrev_b32_e32 v85, 16, v24
	v_and_b32_e32 v86, 0xffff0000, v24
	v_fmac_f32_e32 v81, v83, v85
	v_fmac_f32_e32 v81, v84, v86
	v_lshlrev_b32_e32 v85, 16, v40
	v_and_b32_e32 v86, 0xffff0000, v40
	v_fmac_f32_e32 v82, v83, v85
	v_fmac_f32_e32 v82, v84, v86
	v_lshlrev_b32_e32 v83, 16, v5
	v_and_b32_e32 v84, 0xffff0000, v5
	v_lshlrev_b32_e32 v85, 16, v25
	v_and_b32_e32 v86, 0xffff0000, v25
	v_fmac_f32_e32 v81, v83, v85
	v_fmac_f32_e32 v81, v84, v86
	v_lshlrev_b32_e32 v85, 16, v41
	v_and_b32_e32 v86, 0xffff0000, v41
	v_fmac_f32_e32 v82, v83, v85
	v_fmac_f32_e32 v82, v84, v86
	v_lshlrev_b32_e32 v83, 16, v6
	v_and_b32_e32 v84, 0xffff0000, v6
	v_lshlrev_b32_e32 v85, 16, v26
	v_and_b32_e32 v86, 0xffff0000, v26
	v_fmac_f32_e32 v81, v83, v85
	v_fmac_f32_e32 v81, v84, v86
	v_lshlrev_b32_e32 v85, 16, v42
	v_and_b32_e32 v86, 0xffff0000, v42
	v_fmac_f32_e32 v82, v83, v85
	v_fmac_f32_e32 v82, v84, v86
	v_lshlrev_b32_e32 v83, 16, v7
	v_and_b32_e32 v84, 0xffff0000, v7
	v_lshlrev_b32_e32 v85, 16, v27
	v_and_b32_e32 v86, 0xffff0000, v27
	v_fmac_f32_e32 v81, v83, v85
	v_fmac_f32_e32 v81, v84, v86
	v_lshlrev_b32_e32 v85, 16, v43
	v_and_b32_e32 v86, 0xffff0000, v43
	v_fmac_f32_e32 v82, v83, v85
	v_fmac_f32_e32 v82, v84, v86
	v_lshlrev_b32_e32 v83, 16, v8
	v_and_b32_e32 v84, 0xffff0000, v8
	v_lshlrev_b32_e32 v85, 16, v28
	v_and_b32_e32 v86, 0xffff0000, v28
	v_fmac_f32_e32 v81, v83, v85
	v_fmac_f32_e32 v81, v84, v86
	v_lshlrev_b32_e32 v85, 16, v44
	v_and_b32_e32 v86, 0xffff0000, v44
	v_fmac_f32_e32 v82, v83, v85
	v_fmac_f32_e32 v82, v84, v86
	v_lshlrev_b32_e32 v83, 16, v9
	v_and_b32_e32 v84, 0xffff0000, v9
	v_lshlrev_b32_e32 v85, 16, v29
	v_and_b32_e32 v86, 0xffff0000, v29
	v_fmac_f32_e32 v81, v83, v85
	v_fmac_f32_e32 v81, v84, v86
	v_lshlrev_b32_e32 v85, 16, v45
	v_and_b32_e32 v86, 0xffff0000, v45
	v_fmac_f32_e32 v82, v83, v85
	v_fmac_f32_e32 v82, v84, v86
	v_lshlrev_b32_e32 v83, 16, v10
	v_and_b32_e32 v84, 0xffff0000, v10
	v_lshlrev_b32_e32 v85, 16, v30
	v_and_b32_e32 v86, 0xffff0000, v30
	v_fmac_f32_e32 v81, v83, v85
	v_fmac_f32_e32 v81, v84, v86
	v_lshlrev_b32_e32 v85, 16, v46
	v_and_b32_e32 v86, 0xffff0000, v46
	v_fmac_f32_e32 v82, v83, v85
	v_fmac_f32_e32 v82, v84, v86
	v_lshlrev_b32_e32 v83, 16, v11
	v_and_b32_e32 v84, 0xffff0000, v11
	v_lshlrev_b32_e32 v85, 16, v31
	v_and_b32_e32 v86, 0xffff0000, v31
	v_fmac_f32_e32 v81, v83, v85
	v_fmac_f32_e32 v81, v84, v86
	v_lshlrev_b32_e32 v85, 16, v47
	v_and_b32_e32 v86, 0xffff0000, v47
	v_fmac_f32_e32 v82, v83, v85
	v_fmac_f32_e32 v82, v84, v86
	v_lshlrev_b32_e32 v83, 16, v12
	v_and_b32_e32 v84, 0xffff0000, v12
	v_lshlrev_b32_e32 v85, 16, v32
	v_and_b32_e32 v86, 0xffff0000, v32
	v_fmac_f32_e32 v81, v83, v85
	v_fmac_f32_e32 v81, v84, v86
	v_lshlrev_b32_e32 v85, 16, v48
	v_and_b32_e32 v86, 0xffff0000, v48
	v_fmac_f32_e32 v82, v83, v85
	v_fmac_f32_e32 v82, v84, v86
	v_lshlrev_b32_e32 v83, 16, v13
	v_and_b32_e32 v84, 0xffff0000, v13
	v_lshlrev_b32_e32 v85, 16, v33
	v_and_b32_e32 v86, 0xffff0000, v33
	v_fmac_f32_e32 v81, v83, v85
	v_fmac_f32_e32 v81, v84, v86
	v_lshlrev_b32_e32 v85, 16, v49
	v_and_b32_e32 v86, 0xffff0000, v49
	v_fmac_f32_e32 v82, v83, v85
	v_fmac_f32_e32 v82, v84, v86
	v_lshlrev_b32_e32 v83, 16, v14
	v_and_b32_e32 v84, 0xffff0000, v14
	v_lshlrev_b32_e32 v85, 16, v34
	v_and_b32_e32 v86, 0xffff0000, v34
	v_fmac_f32_e32 v81, v83, v85
	v_fmac_f32_e32 v81, v84, v86
	v_lshlrev_b32_e32 v85, 16, v50
	v_and_b32_e32 v86, 0xffff0000, v50
	v_fmac_f32_e32 v82, v83, v85
	v_fmac_f32_e32 v82, v84, v86
	v_lshlrev_b32_e32 v83, 16, v15
	v_and_b32_e32 v84, 0xffff0000, v15
	v_lshlrev_b32_e32 v85, 16, v35
	v_and_b32_e32 v86, 0xffff0000, v35
	v_fmac_f32_e32 v81, v83, v85
	v_fmac_f32_e32 v81, v84, v86
	v_lshlrev_b32_e32 v85, 16, v51
	v_and_b32_e32 v86, 0xffff0000, v51
	v_fmac_f32_e32 v82, v83, v85
	v_fmac_f32_e32 v82, v84, v86
	v_lshlrev_b32_e32 v83, 16, v16
	v_and_b32_e32 v84, 0xffff0000, v16
	v_lshlrev_b32_e32 v85, 16, v36
	v_and_b32_e32 v86, 0xffff0000, v36
	v_fmac_f32_e32 v81, v83, v85
	v_fmac_f32_e32 v81, v84, v86
	v_lshlrev_b32_e32 v85, 16, v52
	v_and_b32_e32 v86, 0xffff0000, v52
	v_fmac_f32_e32 v82, v83, v85
	v_fmac_f32_e32 v82, v84, v86
	v_lshlrev_b32_e32 v83, 16, v17
	v_and_b32_e32 v84, 0xffff0000, v17
	v_lshlrev_b32_e32 v85, 16, v37
	v_and_b32_e32 v86, 0xffff0000, v37
	v_fmac_f32_e32 v81, v83, v85
	v_fmac_f32_e32 v81, v84, v86
	v_lshlrev_b32_e32 v85, 16, v53
	v_and_b32_e32 v86, 0xffff0000, v53
	v_fmac_f32_e32 v82, v83, v85
	v_fmac_f32_e32 v82, v84, v86
	s_nop 1
	v_add_f32_dpp v81, v81, v81 quad_perm:[1,0,3,2] row_mask:0xf bank_mask:0xf
	s_nop 1
	v_add_f32_dpp v81, v81, v81 quad_perm:[2,3,0,1] row_mask:0xf bank_mask:0xf
	s_nop 1
	v_add_f32_dpp v82, v82, v82 quad_perm:[1,0,3,2] row_mask:0xf bank_mask:0xf
	s_nop 1
	v_add_f32_dpp v82, v82, v82 quad_perm:[2,3,0,1] row_mask:0xf bank_mask:0xf
	s_mov_b32 s38, 0x3db504f3
	s_mov_b32 s40, 0x3fb8aa3b
	s_lshl_b32 s39, s7, 1
	v_mov_b32_e32 v99, 0xff800000
	v_sub_f32_e32 v87, v18, v57
	v_fma_f32 v81, v81, s38, v87
	v_cmp_ge_u32_e32 vcc, s39, v55
	s_nop 1
	v_cndmask_b32_e32 v81, v99, v81, vcc
	v_mov_b32_e32 v88, v81
	s_nop 1
	v_max_f32_dpp v88, v88, v88 row_ror:4 row_mask:0xf bank_mask:0xf
	s_nop 1
	v_max_f32_dpp v88, v88, v88 row_ror:8 row_mask:0xf bank_mask:0xf
	s_nop 1
	v_readlane_b32 s46, v88, 0
	v_readlane_b32 s47, v88, 16
	v_readlane_b32 s48, v88, 32
	v_readlane_b32 s49, v88, 48
	v_mov_b32_e32 v89, s46
	v_max_f32_e32 v89, s47, v89
	v_max_f32_e32 v89, s48, v89
	v_max_f32_e32 v89, s49, v89
	v_sub_f32_e32 v81, v81, v89
	v_mul_f32_e32 v81, s40, v81
	v_exp_f32_e32 v81, v81
	s_nop 0
	v_mov_b32_e32 v90, v81
	s_nop 1
	v_add_f32_dpp v90, v90, v90 row_ror:4 row_mask:0xf bank_mask:0xf
	s_nop 1
	v_add_f32_dpp v90, v90, v90 row_ror:8 row_mask:0xf bank_mask:0xf
	s_nop 1
	v_readlane_b32 s46, v90, 0
	v_readlane_b32 s47, v90, 16
	v_readlane_b32 s48, v90, 32
	v_readlane_b32 s49, v90, 48
	v_mov_b32_e32 v91, s46
	v_add_f32_e32 v91, s47, v91
	v_add_f32_e32 v91, s48, v91
	v_add_f32_e32 v91, s49, v91
	v_readlane_b32 s4, v81, 0
	v_readlane_b32 s5, v81, 4
	v_readlane_b32 s6, v81, 8
	v_readlane_b32 s7, v81, 12
	v_readlane_b32 s8, v81, 16
	v_readlane_b32 s9, v81, 20
	v_readlane_b32 s10, v81, 24
	v_readlane_b32 s11, v81, 28
	v_readlane_b32 s12, v81, 32
	v_readlane_b32 s13, v81, 36
	v_readlane_b32 s14, v81, 40
	v_readlane_b32 s15, v81, 44
	v_readlane_b32 s16, v81, 48
	v_readlane_b32 s17, v81, 52
	v_readlane_b32 s18, v81, 56
	v_readlane_b32 s19, v81, 60
	v_mov_b32_e32 v92, 0
	v_mov_b32_e32 v93, 0
	v_lshlrev_b32_e32 v94, 16, v64
	v_and_b32_e32 v95, 0xffff0000, v64
	v_fmac_f32_e32 v92, s4, v94
	v_fmac_f32_e32 v93, s4, v95
	v_lshlrev_b32_e32 v94, 16, v65
	v_and_b32_e32 v95, 0xffff0000, v65
	v_fmac_f32_e32 v92, s5, v94
	v_fmac_f32_e32 v93, s5, v95
	v_lshlrev_b32_e32 v94, 16, v66
	v_and_b32_e32 v95, 0xffff0000, v66
	v_fmac_f32_e32 v92, s6, v94
	v_fmac_f32_e32 v93, s6, v95
	v_lshlrev_b32_e32 v94, 16, v67
	v_and_b32_e32 v95, 0xffff0000, v67
	v_fmac_f32_e32 v92, s7, v94
	v_fmac_f32_e32 v93, s7, v95
	v_lshlrev_b32_e32 v94, 16, v68
	v_and_b32_e32 v95, 0xffff0000, v68
	v_fmac_f32_e32 v92, s8, v94
	v_fmac_f32_e32 v93, s8, v95
	v_lshlrev_b32_e32 v94, 16, v69
	v_and_b32_e32 v95, 0xffff0000, v69
	v_fmac_f32_e32 v92, s9, v94
	v_fmac_f32_e32 v93, s9, v95
	v_lshlrev_b32_e32 v94, 16, v70
	v_and_b32_e32 v95, 0xffff0000, v70
	v_fmac_f32_e32 v92, s10, v94
	v_fmac_f32_e32 v93, s10, v95
	v_lshlrev_b32_e32 v94, 16, v71
	v_and_b32_e32 v95, 0xffff0000, v71
	v_fmac_f32_e32 v92, s11, v94
	v_fmac_f32_e32 v93, s11, v95
	v_lshlrev_b32_e32 v94, 16, v72
	v_and_b32_e32 v95, 0xffff0000, v72
	v_fmac_f32_e32 v92, s12, v94
	v_fmac_f32_e32 v93, s12, v95
	v_lshlrev_b32_e32 v94, 16, v73
	v_and_b32_e32 v95, 0xffff0000, v73
	v_fmac_f32_e32 v92, s13, v94
	v_fmac_f32_e32 v93, s13, v95
	v_lshlrev_b32_e32 v94, 16, v74
	v_and_b32_e32 v95, 0xffff0000, v74
	v_fmac_f32_e32 v92, s14, v94
	v_fmac_f32_e32 v93, s14, v95
	v_lshlrev_b32_e32 v94, 16, v75
	v_and_b32_e32 v95, 0xffff0000, v75
	v_fmac_f32_e32 v92, s15, v94
	v_fmac_f32_e32 v93, s15, v95
	v_lshlrev_b32_e32 v94, 16, v76
	v_and_b32_e32 v95, 0xffff0000, v76
	v_fmac_f32_e32 v92, s16, v94
	v_fmac_f32_e32 v93, s16, v95
	v_lshlrev_b32_e32 v94, 16, v77
	v_and_b32_e32 v95, 0xffff0000, v77
	v_fmac_f32_e32 v92, s17, v94
	v_fmac_f32_e32 v93, s17, v95
	v_lshlrev_b32_e32 v94, 16, v78
	v_and_b32_e32 v95, 0xffff0000, v78
	v_fmac_f32_e32 v92, s18, v94
	v_fmac_f32_e32 v93, s18, v95
	v_lshlrev_b32_e32 v94, 16, v79
	v_and_b32_e32 v95, 0xffff0000, v79
	v_fmac_f32_e32 v92, s19, v94
	v_fmac_f32_e32 v93, s19, v95
	v_div_scale_f32 v96, s[46:47], v91, v91, 1.0
	v_rcp_f32_e32 v97, v96
	v_div_scale_f32 v98, vcc, 1.0, v91, 1.0
	v_fma_f32 v100, -v96, v97, 1.0
	v_fmac_f32_e32 v97, v100, v97
	v_mul_f32_e32 v100, v98, v97
	v_fma_f32 v101, -v96, v100, v98
	v_fmac_f32_e32 v100, v101, v97
	v_fma_f32 v96, -v96, v100, v98
	s_nop 1
	v_div_fmas_f32 v96, v96, v97, v100
	v_div_fixup_f32 v96, v96, v91, 1.0
	v_cmp_lt_f32_e32 vcc, 0, v91
	s_nop 1
	v_cndmask_b32_e32 v96, 0, v96, vcc
	v_mul_f32_e32 v92, v92, v96
	v_mul_f32_e32 v93, v93, v96
	v_cvt_pk_bf16_f32 v92, v92, v93
	v_lshlrev_b32_e32 v102, 2, v20
	v_add_u32_e32 v102, s34, v102
	global_store_dword v102, v92, s[36:37]
	v_sub_f32_e32 v87, v19, v57
	v_fma_f32 v82, v82, s38, v87
	s_add_i32 s39, s39, 1
	v_cmp_ge_u32_e32 vcc, s39, v55
	s_nop 1
	v_cndmask_b32_e32 v82, v99, v82, vcc
	v_mov_b32_e32 v88, v82
	s_nop 1
	v_max_f32_dpp v88, v88, v88 row_ror:4 row_mask:0xf bank_mask:0xf
	s_nop 1
	v_max_f32_dpp v88, v88, v88 row_ror:8 row_mask:0xf bank_mask:0xf
	s_nop 1
	v_readlane_b32 s46, v88, 0
	v_readlane_b32 s47, v88, 16
	v_readlane_b32 s48, v88, 32
	v_readlane_b32 s49, v88, 48
	v_mov_b32_e32 v89, s46
	v_max_f32_e32 v89, s47, v89
	v_max_f32_e32 v89, s48, v89
	v_max_f32_e32 v89, s49, v89
	v_sub_f32_e32 v82, v82, v89
	v_mul_f32_e32 v82, s40, v82
	v_exp_f32_e32 v82, v82
	s_nop 0
	v_mov_b32_e32 v90, v82
	s_nop 1
	v_add_f32_dpp v90, v90, v90 row_ror:4 row_mask:0xf bank_mask:0xf
	s_nop 1
	v_add_f32_dpp v90, v90, v90 row_ror:8 row_mask:0xf bank_mask:0xf
	s_nop 1
	v_readlane_b32 s46, v90, 0
	v_readlane_b32 s47, v90, 16
	v_readlane_b32 s48, v90, 32
	v_readlane_b32 s49, v90, 48
	v_mov_b32_e32 v91, s46
	v_add_f32_e32 v91, s47, v91
	v_add_f32_e32 v91, s48, v91
	v_add_f32_e32 v91, s49, v91
	v_readlane_b32 s4, v82, 0
	v_readlane_b32 s5, v82, 4
	v_readlane_b32 s6, v82, 8
	v_readlane_b32 s7, v82, 12
	v_readlane_b32 s8, v82, 16
	v_readlane_b32 s9, v82, 20
	v_readlane_b32 s10, v82, 24
	v_readlane_b32 s11, v82, 28
	v_readlane_b32 s12, v82, 32
	v_readlane_b32 s13, v82, 36
	v_readlane_b32 s14, v82, 40
	v_readlane_b32 s15, v82, 44
	v_readlane_b32 s16, v82, 48
	v_readlane_b32 s17, v82, 52
	v_readlane_b32 s18, v82, 56
	v_readlane_b32 s19, v82, 60
	v_mov_b32_e32 v92, 0
	v_mov_b32_e32 v93, 0
	v_lshlrev_b32_e32 v94, 16, v64
	v_and_b32_e32 v95, 0xffff0000, v64
	v_fmac_f32_e32 v92, s4, v94
	v_fmac_f32_e32 v93, s4, v95
	v_lshlrev_b32_e32 v94, 16, v65
	v_and_b32_e32 v95, 0xffff0000, v65
	v_fmac_f32_e32 v92, s5, v94
	v_fmac_f32_e32 v93, s5, v95
	v_lshlrev_b32_e32 v94, 16, v66
	v_and_b32_e32 v95, 0xffff0000, v66
	v_fmac_f32_e32 v92, s6, v94
	v_fmac_f32_e32 v93, s6, v95
	v_lshlrev_b32_e32 v94, 16, v67
	v_and_b32_e32 v95, 0xffff0000, v67
	v_fmac_f32_e32 v92, s7, v94
	v_fmac_f32_e32 v93, s7, v95
	v_lshlrev_b32_e32 v94, 16, v68
	v_and_b32_e32 v95, 0xffff0000, v68
	v_fmac_f32_e32 v92, s8, v94
	v_fmac_f32_e32 v93, s8, v95
	v_lshlrev_b32_e32 v94, 16, v69
	v_and_b32_e32 v95, 0xffff0000, v69
	v_fmac_f32_e32 v92, s9, v94
	v_fmac_f32_e32 v93, s9, v95
	v_lshlrev_b32_e32 v94, 16, v70
	v_and_b32_e32 v95, 0xffff0000, v70
	v_fmac_f32_e32 v92, s10, v94
	v_fmac_f32_e32 v93, s10, v95
	v_lshlrev_b32_e32 v94, 16, v71
	v_and_b32_e32 v95, 0xffff0000, v71
	v_fmac_f32_e32 v92, s11, v94
	v_fmac_f32_e32 v93, s11, v95
	v_lshlrev_b32_e32 v94, 16, v72
	v_and_b32_e32 v95, 0xffff0000, v72
	v_fmac_f32_e32 v92, s12, v94
	v_fmac_f32_e32 v93, s12, v95
	v_lshlrev_b32_e32 v94, 16, v73
	v_and_b32_e32 v95, 0xffff0000, v73
	v_fmac_f32_e32 v92, s13, v94
	v_fmac_f32_e32 v93, s13, v95
	v_lshlrev_b32_e32 v94, 16, v74
	v_and_b32_e32 v95, 0xffff0000, v74
	v_fmac_f32_e32 v92, s14, v94
	v_fmac_f32_e32 v93, s14, v95
	v_lshlrev_b32_e32 v94, 16, v75
	v_and_b32_e32 v95, 0xffff0000, v75
	v_fmac_f32_e32 v92, s15, v94
	v_fmac_f32_e32 v93, s15, v95
	v_lshlrev_b32_e32 v94, 16, v76
	v_and_b32_e32 v95, 0xffff0000, v76
	v_fmac_f32_e32 v92, s16, v94
	v_fmac_f32_e32 v93, s16, v95
	v_lshlrev_b32_e32 v94, 16, v77
	v_and_b32_e32 v95, 0xffff0000, v77
	v_fmac_f32_e32 v92, s17, v94
	v_fmac_f32_e32 v93, s17, v95
	v_lshlrev_b32_e32 v94, 16, v78
	v_and_b32_e32 v95, 0xffff0000, v78
	v_fmac_f32_e32 v92, s18, v94
	v_fmac_f32_e32 v93, s18, v95
	v_lshlrev_b32_e32 v94, 16, v79
	v_and_b32_e32 v95, 0xffff0000, v79
	v_fmac_f32_e32 v92, s19, v94
	v_fmac_f32_e32 v93, s19, v95
	v_div_scale_f32 v96, s[46:47], v91, v91, 1.0
	v_rcp_f32_e32 v97, v96
	v_div_scale_f32 v98, vcc, 1.0, v91, 1.0
	v_fma_f32 v100, -v96, v97, 1.0
	v_fmac_f32_e32 v97, v100, v97
	v_mul_f32_e32 v100, v98, v97
	v_fma_f32 v101, -v96, v100, v98
	v_fmac_f32_e32 v100, v101, v97
	v_fma_f32 v96, -v96, v100, v98
	s_nop 1
	v_div_fmas_f32 v96, v96, v97, v100
	v_div_fixup_f32 v96, v96, v91, 1.0
	v_cmp_lt_f32_e32 vcc, 0, v91
	s_nop 1
	v_cndmask_b32_e32 v96, 0, v96, vcc
	v_mul_f32_e32 v92, v92, v96
	v_mul_f32_e32 v93, v93, v96
	v_cvt_pk_bf16_f32 v92, v92, v93
	v_lshlrev_b32_e32 v102, 2, v20
	s_add_i32 s34, s34, 0x1000
	v_add_u32_e32 v102, s34, v102
	global_store_dword v102, v92, s[36:37]
	s_branch .LBB0_1259
